# H1 stage 2 first four steps: six b128 LDS reads issued up front into v[184:199], MFMAs back to back, convert/store tails after the next chain's reads are in flight
# baseline (speedup 1.0000x reference)
.LBB0_564:
	s_waitcnt lgkmcnt(0)
	s_barrier
	ds_read_b64_tr_b16 v[16:17], v131
	ds_read_b64_tr_b16 v[18:19], v131 offset:1088
	ds_read_b64_tr_b16 v[12:13], v131 offset:8704
	ds_read_b64_tr_b16 v[14:15], v131 offset:9792
	ds_read_b128 v[20:23], v132
	ds_read_b128 v[184:187], v132 offset:2304
	ds_read_b128 v[188:191], v132 offset:4608
	ds_read_b128 v[24:27], v132 offset:4672
	ds_read_b128 v[192:195], v132 offset:6912
	ds_read_b128 v[196:199], v132 offset:6976
	s_mov_b32 s39, 0x10000
	v_add_u32_e32 v59, v114, v115
	s_waitcnt vmcnt(24)
	v_mov_b32_e32 v100, v134
	s_waitcnt vmcnt(22)
	v_mov_b32_e32 v148, v135
	s_waitcnt lgkmcnt(5)
	v_mfma_f32_16x16x32_bf16 v[20:23], v[16:19], v[20:23], 0
	s_waitcnt vmcnt(20)
	v_mov_b32_e32 v147, v136
	s_waitcnt vmcnt(18)
	v_mov_b32_e32 v146, v137
	s_waitcnt vmcnt(16)
	v_mov_b32_e32 v145, v138
	s_waitcnt vmcnt(14)
	v_mov_b32_e32 v144, v139
	s_waitcnt vmcnt(13)
	v_mov_b32_e32 v143, v140
	s_waitcnt lgkmcnt(4)
	v_mfma_f32_16x16x32_bf16 v[184:187], v[16:19], v[184:187], 0
	s_waitcnt lgkmcnt(2)
	v_mfma_f32_16x16x32_bf16 v[188:191], v[16:19], v[188:191], 0
	v_mfma_f32_16x16x32_bf16 v[188:191], v[12:15], v[24:27], v[188:191]
	s_waitcnt lgkmcnt(0)
	v_mfma_f32_16x16x32_bf16 v[192:195], v[16:19], v[192:195], 0
	v_mfma_f32_16x16x32_bf16 v[192:195], v[12:15], v[196:199], v[192:195]
	ds_read_b64_tr_b16 v[152:153], v59 offset:60928
	ds_read_b64_tr_b16 v[154:155], v59 offset:62016
	ds_read_b64_tr_b16 v[156:157], v133 offset:60928
	ds_read_b64_tr_b16 v[158:159], v133 offset:62016
	ds_read_b64_tr_b16 v[160:161], v59 offset:60960
	ds_read_b64_tr_b16 v[162:163], v59 offset:62048
	ds_read_b64_tr_b16 v[164:165], v133 offset:60960
	ds_read_b64_tr_b16 v[166:167], v133 offset:62048
	ds_read_b64_tr_b16 v[168:169], v59 offset:60992
	ds_read_b64_tr_b16 v[170:171], v59 offset:62080
	ds_read_b64_tr_b16 v[172:173], v133 offset:60992
	ds_read_b64_tr_b16 v[174:175], v133 offset:62080
	v_cvt_pk_bf16_f32 v20, v20, v21
	v_cvt_pk_bf16_f32 v21, v22, v23
	v_lshl_add_u64 v[22:23], s[78:79], 1, v[54:55]
	v_lshl_add_u64 v[22:23], s[54:55], 1, v[22:23]
	v_lshl_add_u64 v[60:61], v[22:23], 0, v[2:3]
	global_store_dwordx2 v[60:61], v[20:21], off
	v_readlane_b32 s78, v250, 1
	s_waitcnt vmcnt(12)
	v_mov_b32_e32 v142, v141
	s_mov_b32 s82, s81
	v_cvt_pk_bf16_f32 v20, v184, v185
	v_cvt_pk_bf16_f32 v21, v186, v187
	v_add_co_u32_e32 v22, vcc, s39, v60
	s_mov_b32 s39, 0x20000
	s_nop 0
	v_addc_co_u32_e32 v23, vcc, 0, v61, vcc
	global_store_dwordx2 v[22:23], v[20:21], off
	v_readlane_b32 s79, v250, 2
	v_cvt_pk_bf16_f32 v20, v188, v189
	v_cvt_pk_bf16_f32 v21, v190, v191
	v_add_co_u32_e32 v22, vcc, s39, v60
	s_mov_b32 s39, 0x30000
	s_nop 0
	v_addc_co_u32_e32 v23, vcc, 0, v61, vcc
	global_store_dwordx2 v[22:23], v[20:21], off
	v_cvt_pk_bf16_f32 v20, v192, v193
	v_cvt_pk_bf16_f32 v21, v194, v195
	v_add_co_u32_e32 v22, vcc, s39, v60
	s_ashr_i32 s39, s38, 31
	s_nop 0
	v_addc_co_u32_e32 v23, vcc, 0, v61, vcc
	global_store_dwordx2 v[22:23], v[20:21], off
	s_lshl_b64 s[38:39], s[38:39], 15
	s_and_b64 vcc, exec, s[76:77]
	v_lshl_add_u64 v[20:21], v[56:57], 0, s[38:39]
	s_waitcnt lgkmcnt(8)
	v_mfma_f32_16x16x32_bf16 v[152:155], v[152:155], v[16:19], 0
	v_mfma_f32_16x16x32_bf16 v[152:155], v[156:159], v[12:15], v[152:155]
	ds_read_b64_tr_b16 v[176:177], v59 offset:61024
	ds_read_b64_tr_b16 v[178:179], v59 offset:62112
	ds_read_b64_tr_b16 v[180:181], v133 offset:61024
	ds_read_b64_tr_b16 v[182:183], v133 offset:62112
	s_waitcnt lgkmcnt(8)
	v_mfma_f32_16x16x32_bf16 v[160:163], v[160:163], v[16:19], 0
	v_mfma_f32_16x16x32_bf16 v[160:163], v[164:167], v[12:15], v[160:163]
	s_nop 1
	v_cvt_pk_bf16_f32 v22, v152, v153
	v_cvt_pk_bf16_f32 v23, v154, v155
	global_store_dwordx2 v[20:21], v[22:23], off
	ds_read_b64_tr_b16 v[152:153], v59 offset:61056
	ds_read_b64_tr_b16 v[154:155], v59 offset:62144
	ds_read_b64_tr_b16 v[156:157], v133 offset:61056
	ds_read_b64_tr_b16 v[158:159], v133 offset:62144
	s_waitcnt lgkmcnt(8)
	v_mfma_f32_16x16x32_bf16 v[168:171], v[168:171], v[16:19], 0
	v_mfma_f32_16x16x32_bf16 v[168:171], v[172:175], v[12:15], v[168:171]
	s_nop 1
	v_cvt_pk_bf16_f32 v22, v160, v161
	v_cvt_pk_bf16_f32 v23, v162, v163
	global_store_dwordx2 v[20:21], v[22:23], off offset:32
	ds_read_b64_tr_b16 v[160:161], v59 offset:61088
	ds_read_b64_tr_b16 v[162:163], v59 offset:62176
	ds_read_b64_tr_b16 v[164:165], v133 offset:61088
	ds_read_b64_tr_b16 v[166:167], v133 offset:62176
	s_waitcnt lgkmcnt(8)
	v_mfma_f32_16x16x32_bf16 v[176:179], v[176:179], v[16:19], 0
	v_mfma_f32_16x16x32_bf16 v[176:179], v[180:183], v[12:15], v[176:179]
	s_nop 1
	v_cvt_pk_bf16_f32 v22, v168, v169
	v_cvt_pk_bf16_f32 v23, v170, v171
	global_store_dwordx2 v[20:21], v[22:23], off offset:64
	ds_read_b64_tr_b16 v[168:169], v59 offset:61120
	ds_read_b64_tr_b16 v[170:171], v59 offset:62208
	ds_read_b64_tr_b16 v[172:173], v133 offset:61120
	ds_read_b64_tr_b16 v[174:175], v133 offset:62208
	s_waitcnt lgkmcnt(8)
	v_mfma_f32_16x16x32_bf16 v[152:155], v[152:155], v[16:19], 0
	v_mfma_f32_16x16x32_bf16 v[152:155], v[156:159], v[12:15], v[152:155]
	s_nop 1
	v_cvt_pk_bf16_f32 v22, v176, v177
	v_cvt_pk_bf16_f32 v23, v178, v179
	global_store_dwordx2 v[20:21], v[22:23], off offset:96
	ds_read_b64_tr_b16 v[176:177], v59 offset:61152
	ds_read_b64_tr_b16 v[178:179], v59 offset:62240
	ds_read_b64_tr_b16 v[180:181], v133 offset:61152
	ds_read_b64_tr_b16 v[182:183], v133 offset:62240
	s_waitcnt lgkmcnt(8)
	v_mfma_f32_16x16x32_bf16 v[160:163], v[160:163], v[16:19], 0
	v_mfma_f32_16x16x32_bf16 v[160:163], v[164:167], v[12:15], v[160:163]
	s_nop 1
	v_cvt_pk_bf16_f32 v22, v152, v153
	v_cvt_pk_bf16_f32 v23, v154, v155
	global_store_dwordx2 v[20:21], v[22:23], off offset:128
	s_waitcnt lgkmcnt(4)
	v_mfma_f32_16x16x32_bf16 v[168:171], v[168:171], v[16:19], 0
	v_mfma_f32_16x16x32_bf16 v[168:171], v[172:175], v[12:15], v[168:171]
	s_nop 1
	v_cvt_pk_bf16_f32 v22, v160, v161
	v_cvt_pk_bf16_f32 v23, v162, v163
	global_store_dwordx2 v[20:21], v[22:23], off offset:160
	s_waitcnt lgkmcnt(0)
	v_mfma_f32_16x16x32_bf16 v[176:179], v[176:179], v[16:19], 0
	v_mfma_f32_16x16x32_bf16 v[176:179], v[180:183], v[12:15], v[176:179]
	s_nop 1
	v_cvt_pk_bf16_f32 v22, v168, v169
	v_cvt_pk_bf16_f32 v23, v170, v171
	global_store_dwordx2 v[20:21], v[22:23], off offset:192
	s_nop 7
	s_nop 1
	v_cvt_pk_bf16_f32 v22, v176, v177
	v_cvt_pk_bf16_f32 v23, v178, v179
	global_store_dwordx2 v[20:21], v[22:23], off offset:224
	s_waitcnt lgkmcnt(0)
	s_barrier
	s_cbranch_vccnz .LBB0_648
